# grid barrier: the now unread release word TOPGEN is no longer bumped, so the last-arriving XCD leader does not wait (vmcnt) for that device-scope atomic before releasing its own XCD
# speedup vs baseline: 1.0154x; 1.0071x over previous
.LBB0_219:
	s_or_b64 exec, exec, s[4:5]
	s_and_saveexec_b64 s[4:5], s[8:9]
	s_cbranch_execz .LBB0_221
	v_mov_b32_e32 v2, 1
	s_nop 0

.LBB0_295:
	s_or_b64 exec, exec, s[6:7]
	s_and_saveexec_b64 s[6:7], s[10:11]
	s_cbranch_execz .LBB0_297
	v_mov_b32_e32 v2, 1
	s_nop 0

.LBB0_719:
	s_or_b64 exec, exec, s[4:5]
	s_and_saveexec_b64 s[4:5], s[10:11]
	s_cbranch_execz .LBB0_721
	v_mov_b32_e32 v2, 1
	s_nop 0

.LBB0_789:
	s_or_b64 exec, exec, s[4:5]
	s_and_saveexec_b64 s[4:5], s[12:13]
	s_cbranch_execz .LBB0_791
	v_mov_b32_e32 v2, 1
	s_nop 0

.LBB0_887:
	s_or_b64 exec, exec, s[4:5]
	s_and_saveexec_b64 s[4:5], s[14:15]
	s_cbranch_execz .LBB0_889
	v_mov_b32_e32 v2, 1
	s_nop 0

.LBB0_977:
	s_or_b64 exec, exec, s[6:7]
	s_and_saveexec_b64 s[6:7], s[14:15]
	s_cbranch_execz .LBB0_979
	v_mov_b32_e32 v2, 1
	s_nop 0
